# P9: first two counted waits allow the 4 extra loads in the gather/bias iterations (vmcnt 12), row-index prefetch unconditional (clamped)
# baseline (speedup 1.0000x reference)
.LBB0_1355:
	s_cmp_eq_u32 s29, -2
	s_cbranch_scc1 .Lp9_peel
	v_add_u32_e32 v2, s85, v185
	v_add_u32_e32 v14, s86, v185
	ds_read_b128 v[18:21], v2
	ds_read_b128 v[22:25], v2 offset:1024
	ds_read_b128 v[26:29], v2 offset:2048
	ds_read_b128 v[30:33], v2 offset:3072
	ds_read_b128 v[2:5], v14
	ds_read_b128 v[6:9], v14 offset:1024
	ds_read_b128 v[10:13], v14 offset:2048
	ds_read_b128 v[14:17], v14 offset:3072
	v_lshl_add_u64 v[222:223], s[50:51], 0, v[168:169]
	s_add_i32 m0, s59, 0xc000
	ds_read_b128 v[174:177], v188
	ds_read_b128 v[178:181], v188 offset:1024
	ds_read_b128 v[198:201], v188 offset:2048
	ds_read_b128 v[202:205], v188 offset:3072
	ds_read_b128 v[206:209], v188 offset:4096
	ds_read_b128 v[210:213], v188 offset:5120
	ds_read_b128 v[214:217], v188 offset:6144
	ds_read_b128 v[218:221], v188 offset:7168
	global_load_lds_dwordx4 v[222:223], off
	v_lshl_add_u64 v[222:223], s[50:51], 0, v[172:173]
	s_add_i32 m0, s59, 0xe000
	s_nop 0
	global_load_lds_dwordx4 v[222:223], off
	s_cmp_lt_i32 s29, 10
	s_cbranch_scc1 .Lp9_was
	s_cmp_eq_u32 s29, 12
	s_cbranch_scc1 .Lp9_wa
	s_cmp_lg_u64 s[4:5], 0
	s_cbranch_scc1 .Lp9_wa

.Lp9_wa:
	s_waitcnt vmcnt(12)
	s_waitcnt lgkmcnt(0)
	s_barrier
	s_setprio 1
	s_waitcnt lgkmcnt(0)
	v_mfma_f32_16x16x128_f8f6f4 v[158:161], v[18:25], v[174:181], v[158:161]
	v_mfma_f32_16x16x128_f8f6f4 v[154:157], v[26:33], v[174:181], v[154:157]
	v_mfma_f32_16x16x128_f8f6f4 v[142:145], v[18:25], v[198:205], v[142:145]
	v_mfma_f32_16x16x128_f8f6f4 v[134:137], v[26:33], v[198:205], v[134:137]
	v_mfma_f32_16x16x128_f8f6f4 v[126:129], v[18:25], v[206:213], v[126:129]
	v_mfma_f32_16x16x128_f8f6f4 v[118:121], v[26:33], v[206:213], v[118:121]
	v_mfma_f32_16x16x128_f8f6f4 v[110:113], v[18:25], v[214:221], v[110:113]
	v_mfma_f32_16x16x128_f8f6f4 v[102:105], v[26:33], v[214:221], v[102:105]
	s_setprio 0
	s_setprio 1
	v_mfma_f32_16x16x128_f8f6f4 v[150:153], v[2:9], v[174:181], v[150:153]
	v_mfma_f32_16x16x128_f8f6f4 v[146:149], v[10:17], v[174:181], v[146:149]
	v_mfma_f32_16x16x128_f8f6f4 v[138:141], v[2:9], v[198:205], v[138:141]
	v_mfma_f32_16x16x128_f8f6f4 v[130:133], v[10:17], v[198:205], v[130:133]
	v_mfma_f32_16x16x128_f8f6f4 v[122:125], v[2:9], v[206:213], v[122:125]
	v_mfma_f32_16x16x128_f8f6f4 v[114:117], v[10:17], v[206:213], v[114:117]
	v_mfma_f32_16x16x128_f8f6f4 v[106:109], v[2:9], v[214:221], v[106:109]
	v_mfma_f32_16x16x128_f8f6f4 v[98:101], v[10:17], v[214:221], v[98:101]
	s_setprio 0
	s_barrier
	s_add_i32 s37, s85, s58
	v_lshl_add_u64 v[174:175], s[46:47], 0, v[164:165]
	s_mov_b32 m0, s37
	ds_read_b128 v[198:201], v188 offset:16384
	ds_read_b128 v[202:205], v188 offset:17408
	ds_read_b128 v[206:209], v188 offset:18432
	ds_read_b128 v[210:213], v188 offset:19456
	ds_read_b128 v[214:217], v188 offset:20480
	ds_read_b128 v[218:221], v188 offset:21504
	ds_read_b128 v[222:225], v188 offset:22528
	ds_read_b128 v[226:229], v188 offset:23552
	global_load_lds_dwordx4 v[174:175], off
	s_add_i32 m0, s37, 0x2000
	s_add_u32 s50, s46, 0x40000
	v_lshl_add_u64 v[176:177], s[46:47], 0, v[166:167]
	s_addc_u32 s51, s47, 0
	s_add_i32 s37, s86, s58
	global_load_lds_dwordx4 v[176:177], off
	v_lshl_add_u64 v[178:179], s[50:51], 0, v[164:165]
	s_mov_b32 m0, s37
	v_cndmask_b32_e64 v162, v196, v192, s[6:7]
	global_load_lds_dwordx4 v[178:179], off
	v_lshl_add_u64 v[178:179], s[50:51], 0, v[166:167]
	s_add_i32 m0, s37, 0x2000
	s_nop 0
	global_load_lds_dwordx4 v[178:179], off
	s_mov_b32 m0, s59
	v_lshl_add_u64 v[178:179], s[48:49], 0, v[162:163]
	global_load_lds_dwordx4 v162, s[48:49]
	v_cndmask_b32_e64 v162, v170, v191, s[6:7]
	s_mov_b32 m0, s60
	v_lshl_add_u64 v[180:181], s[48:49], 0, v[162:163]
	global_load_lds_dwordx4 v162, s[48:49]
	s_cmp_lt_i32 s29, 10
	s_cbranch_scc1 .Lp9_wbs
	s_cmp_eq_u32 s29, 12
	s_cbranch_scc1 .Lp9_wb
	s_cmp_lg_u64 s[4:5], 0
	s_cbranch_scc1 .Lp9_wb

.Lp9_wb:
	s_waitcnt vmcnt(12)
	s_waitcnt lgkmcnt(0)
	s_barrier
	s_setprio 1
	s_waitcnt lgkmcnt(0)
	v_mfma_f32_16x16x128_f8f6f4 v[94:97], v[18:25], v[198:205], v[94:97]
	v_mfma_f32_16x16x128_f8f6f4 v[86:89], v[26:33], v[198:205], v[86:89]
	v_mfma_f32_16x16x128_f8f6f4 v[78:81], v[18:25], v[206:213], v[78:81]
	v_mfma_f32_16x16x128_f8f6f4 v[70:73], v[26:33], v[206:213], v[70:73]
	v_mfma_f32_16x16x128_f8f6f4 v[62:65], v[18:25], v[214:221], v[62:65]
	v_mfma_f32_16x16x128_f8f6f4 v[54:57], v[26:33], v[214:221], v[54:57]
	v_mfma_f32_16x16x128_f8f6f4 v[46:49], v[18:25], v[222:229], v[46:49]
	v_mfma_f32_16x16x128_f8f6f4 v[38:41], v[26:33], v[222:229], v[38:41]
	s_setprio 0
	s_setprio 1
	v_mfma_f32_16x16x128_f8f6f4 v[90:93], v[2:9], v[198:205], v[90:93]
	v_mfma_f32_16x16x128_f8f6f4 v[82:85], v[10:17], v[198:205], v[82:85]
	v_mfma_f32_16x16x128_f8f6f4 v[74:77], v[2:9], v[206:213], v[74:77]
	v_mfma_f32_16x16x128_f8f6f4 v[66:69], v[10:17], v[206:213], v[66:69]
	v_mfma_f32_16x16x128_f8f6f4 v[58:61], v[2:9], v[214:221], v[58:61]
	v_mfma_f32_16x16x128_f8f6f4 v[50:53], v[10:17], v[214:221], v[50:53]
	v_mfma_f32_16x16x128_f8f6f4 v[42:45], v[2:9], v[222:229], v[42:45]
	v_mfma_f32_16x16x128_f8f6f4 v[34:37], v[10:17], v[222:229], v[34:37]
	s_setprio 0
	s_barrier
	s_add_i32 s37, 0, 0x18000
	s_add_i32 s50, 0, 0x1c000
	v_add_u32_e32 v14, s37, v185
	v_add_u32_e32 v30, s50, v185
	ds_read_b128 v[2:5], v14
	ds_read_b128 v[6:9], v14 offset:1024
	ds_read_b128 v[10:13], v14 offset:2048
	ds_read_b128 v[14:17], v14 offset:3072
	ds_read_b128 v[18:21], v30
	ds_read_b128 v[22:25], v30 offset:1024
	ds_read_b128 v[26:29], v30 offset:2048
	ds_read_b128 v[30:33], v30 offset:3072
	s_mov_b32 m0, s61
	v_cndmask_b32_e64 v162, v168, v190, s[6:7]
	ds_read_b128 v[198:201], v188 offset:32768
	ds_read_b128 v[202:205], v188 offset:33792
	ds_read_b128 v[206:209], v188 offset:34816
	ds_read_b128 v[210:213], v188 offset:35840
	ds_read_b128 v[214:217], v188 offset:36864
	ds_read_b128 v[218:221], v188 offset:37888
	ds_read_b128 v[222:225], v188 offset:38912
	ds_read_b128 v[226:229], v188 offset:39936
	global_load_lds_dwordx4 v162, s[48:49]
	v_cndmask_b32_e64 v162, v172, v193, s[6:7]
	s_mov_b32 m0, s62
	s_nop 0
	global_load_lds_dwordx4 v162, s[48:49]
	s_waitcnt vmcnt(8)
	s_waitcnt lgkmcnt(0)
	s_barrier
	s_setprio 1
	s_waitcnt lgkmcnt(0)
	v_mfma_f32_16x16x128_f8f6f4 v[158:161], v[2:9], v[198:205], v[158:161]
	v_mfma_f32_16x16x128_f8f6f4 v[154:157], v[10:17], v[198:205], v[154:157]
	v_mfma_f32_16x16x128_f8f6f4 v[142:145], v[2:9], v[206:213], v[142:145]
	v_mfma_f32_16x16x128_f8f6f4 v[134:137], v[10:17], v[206:213], v[134:137]
	v_mfma_f32_16x16x128_f8f6f4 v[126:129], v[2:9], v[214:221], v[126:129]
	v_mfma_f32_16x16x128_f8f6f4 v[118:121], v[10:17], v[214:221], v[118:121]
	v_mfma_f32_16x16x128_f8f6f4 v[110:113], v[2:9], v[222:229], v[110:113]
	v_mfma_f32_16x16x128_f8f6f4 v[102:105], v[10:17], v[222:229], v[102:105]
	s_setprio 0
	s_setprio 1
	v_mfma_f32_16x16x128_f8f6f4 v[150:153], v[18:25], v[198:205], v[150:153]
	v_mfma_f32_16x16x128_f8f6f4 v[146:149], v[26:33], v[198:205], v[146:149]
	v_mfma_f32_16x16x128_f8f6f4 v[138:141], v[18:25], v[206:213], v[138:141]
	v_mfma_f32_16x16x128_f8f6f4 v[130:133], v[26:33], v[206:213], v[130:133]
	v_mfma_f32_16x16x128_f8f6f4 v[122:125], v[18:25], v[214:221], v[122:125]
	v_mfma_f32_16x16x128_f8f6f4 v[114:117], v[26:33], v[214:221], v[114:117]
	v_mfma_f32_16x16x128_f8f6f4 v[106:109], v[18:25], v[222:229], v[106:109]
	v_mfma_f32_16x16x128_f8f6f4 v[98:101], v[26:33], v[222:229], v[98:101]
	s_setprio 0
	s_barrier
	s_add_i32 s6, s37, s58
	v_lshl_add_u64 v[174:175], v[174:175], 0, s[16:17]
	s_mov_b32 m0, s6
	ds_read_b128 v[198:201], v188 offset:49152
	ds_read_b128 v[202:205], v188 offset:50176
	ds_read_b128 v[206:209], v188 offset:51200
	ds_read_b128 v[210:213], v188 offset:52224
	ds_read_b128 v[214:217], v188 offset:53248
	ds_read_b128 v[218:221], v188 offset:54272
	ds_read_b128 v[222:225], v188 offset:55296
	ds_read_b128 v[226:229], v188 offset:56320
	global_load_lds_dwordx4 v[174:175], off
	s_add_i32 m0, s6, 0x2000
	s_add_u32 s6, s46, 0x40080
	v_lshl_add_u64 v[174:175], v[176:177], 0, s[16:17]
	s_addc_u32 s7, s47, 0
	s_add_i32 s37, s50, s58
	global_load_lds_dwordx4 v[174:175], off
	v_lshl_add_u64 v[174:175], s[6:7], 0, v[164:165]
	s_mov_b32 m0, s37
	s_nop 0
	global_load_lds_dwordx4 v[174:175], off
	v_lshl_add_u64 v[174:175], s[6:7], 0, v[166:167]
	s_add_i32 m0, s37, 0x2000
	s_nop 0
	global_load_lds_dwordx4 v[174:175], off
	v_lshl_add_u64 v[174:175], v[178:179], 0, s[16:17]
	s_mov_b32 m0, s66
	s_nop 0
	global_load_lds_dwordx4 v[174:175], off
	v_lshl_add_u64 v[174:175], v[180:181], 0, s[16:17]
	s_mov_b32 m0, s67
	s_nop 0
	global_load_lds_dwordx4 v[174:175], off
	s_waitcnt vmcnt(8)
	s_waitcnt lgkmcnt(0)
	s_barrier
	s_setprio 1
	s_waitcnt lgkmcnt(0)
	v_mfma_f32_16x16x128_f8f6f4 v[94:97], v[2:9], v[198:205], v[94:97]
	v_mfma_f32_16x16x128_f8f6f4 v[86:89], v[10:17], v[198:205], v[86:89]
	v_mfma_f32_16x16x128_f8f6f4 v[78:81], v[2:9], v[206:213], v[78:81]
	v_mfma_f32_16x16x128_f8f6f4 v[70:73], v[10:17], v[206:213], v[70:73]
	v_mfma_f32_16x16x128_f8f6f4 v[62:65], v[2:9], v[214:221], v[62:65]
	v_mfma_f32_16x16x128_f8f6f4 v[54:57], v[10:17], v[214:221], v[54:57]
	v_mfma_f32_16x16x128_f8f6f4 v[46:49], v[2:9], v[222:229], v[46:49]
	v_mfma_f32_16x16x128_f8f6f4 v[38:41], v[10:17], v[222:229], v[38:41]
	s_setprio 0
	s_setprio 1
	v_mfma_f32_16x16x128_f8f6f4 v[90:93], v[18:25], v[198:205], v[90:93]
	v_mfma_f32_16x16x128_f8f6f4 v[82:85], v[26:33], v[198:205], v[82:85]
	v_mfma_f32_16x16x128_f8f6f4 v[74:77], v[18:25], v[206:213], v[74:77]
	v_mfma_f32_16x16x128_f8f6f4 v[66:69], v[26:33], v[206:213], v[66:69]
	v_mfma_f32_16x16x128_f8f6f4 v[58:61], v[18:25], v[214:221], v[58:61]
	v_mfma_f32_16x16x128_f8f6f4 v[50:53], v[26:33], v[214:221], v[50:53]
	v_mfma_f32_16x16x128_f8f6f4 v[42:45], v[18:25], v[222:229], v[42:45]
	v_mfma_f32_16x16x128_f8f6f4 v[34:37], v[26:33], v[222:229], v[34:37]
	s_setprio 0
	s_barrier
	s_add_i32 s29, s29, 2
	s_add_u32 s44, s44, 0x100
	s_addc_u32 s45, s45, 0
	s_add_u32 s38, s38, 0x100
	s_addc_u32 s39, s39, 0
	s_cmp_gt_u32 s29, 13
	s_cbranch_scc1 .LBB0_1368

.Lp9_nobias:
	s_cmp_lg_u32 s29, 10
	s_cbranch_scc1 .LBB0_1355
	s_andn2_b64 vcc, exec, s[4:5]
	v_mov_b32_e32 v192, v196
	v_mov_b32_e32 v191, v170
	v_mov_b32_e32 v190, v168
	v_mov_b32_e32 v193, v172
	s_cbranch_vccnz .LBB0_1355
	v_mov_b32_e32 v2, s27
	ds_read2st64_b32 v[2:3], v2 offset1:1
	v_mov_b32_e32 v230, 0
	v_mov_b32_e32 v231, 0
	v_mov_b32_e32 v232, 0
	v_mov_b32_e32 v233, 0
	s_waitcnt lgkmcnt(0)
	v_add_u32_e32 v197, -1, v3
	v_sub_u32_e32 v2, v194, v2
	v_lshlrev_b32_e32 v2, 8, v2
	v_add_u32_e32 v4, v2, v1
	v_min_i32_e32 v4, v4, v197
	v_ashrrev_i32_e32 v5, 31, v4
	v_lshl_add_u64 v[4:5], v[4:5], 2, s[42:43]
	global_load_dword v230, v[4:5], off
	v_add_u32_e32 v4, v2, v182
	v_min_i32_e32 v4, v4, v197
	v_ashrrev_i32_e32 v5, 31, v4
	v_lshl_add_u64 v[4:5], v[4:5], 2, s[42:43]
	global_load_dword v231, v[4:5], off
	v_or_b32_e32 v2, 0x80, v2
	v_add_u32_e32 v4, v2, v1
	v_min_i32_e32 v4, v4, v197
	v_ashrrev_i32_e32 v5, 31, v4
	v_lshl_add_u64 v[4:5], v[4:5], 2, s[42:43]
	global_load_dword v232, v[4:5], off
	v_add_u32_e32 v2, v2, v182
	v_min_i32_e32 v2, v2, v197
	v_ashrrev_i32_e32 v3, 31, v2
	v_lshl_add_u64 v[2:3], v[2:3], 2, s[42:43]
	global_load_dword v233, v[2:3], off
	s_branch .LBB0_1355
